# full-tile attention loops: straight-line rescale test, dropped self-max canonicalisations and +0 adds
# speedup vs baseline: 1.0164x; 1.0025x over previous
.LBB0_695:
	v_add_f32_e32 v2, v208, v2
	v_add_f32_e32 v4, v209, v66
	v_add_f32_e32 v2, v4, v2
	v_add_f32_e32 v4, v84, v67
	v_add_f32_e32 v2, v4, v2
	v_add_f32_e32 v4, v85, v68
	v_add_f32_e32 v2, v4, v2
	v_add_f32_e32 v4, v86, v69
	v_add_f32_e32 v2, v4, v2
	v_add_f32_e32 v4, v87, v70
	v_add_f32_e32 v2, v4, v2
	v_add_f32_e32 v4, v88, v71
	v_add_f32_e32 v2, v4, v2
	v_add_f32_e32 v4, v89, v72
	v_add_f32_e32 v2, v4, v2
	v_add_f32_e32 v4, v90, v73
	v_add_f32_e32 v2, v4, v2
	v_add_f32_e32 v4, v91, v74
	v_add_f32_e32 v2, v4, v2
	v_add_f32_e32 v4, v95, v75
	v_add_f32_e32 v2, v4, v2
	v_add_f32_e32 v4, v77, v82
	v_add_f32_e32 v2, v4, v2
	v_add_f32_e32 v4, v76, v83
	v_add_f32_e32 v2, v4, v2
	v_add_f32_e32 v4, v96, v94
	v_add_f32_e32 v2, v4, v2
	v_add_f32_e32 v4, v79, v93
	s_add_i32 s10, s60, 1
	v_add_f32_e32 v2, v4, v2
	v_add_f32_e32 v4, v78, v92
	s_and_b32 s60, s10, 3
	s_waitcnt vmcnt(6) lgkmcnt(0)
	s_barrier
	s_add_i32 s10, s64, 1
	v_add_f32_e32 v2, v4, v2
	s_and_b32 s64, s10, 3
	s_add_i32 s73, s73, 1
	v_add_f32_e32 v191, v191, v2
	s_cmp_eq_u32 s71, s73
	s_cbranch_scc1 .LBB0_741

.LBB0_719:
	s_mul_i32 s26, s64, 0x5400
	s_add_i32 s26, s26, 0
	v_add_u32_e32 v2, s26, v205
	v_and_b32_e32 v4, 64, v242
	v_add_u32_e32 v17, 64, v4
	s_waitcnt lgkmcnt(3)
	ds_read_b128 v[4:7], v2
	s_waitcnt lgkmcnt(1)
	ds_read_b128 v[8:11], v2 offset:32
	ds_read_b128 v[12:15], v2 offset:6656
	ds_read_b128 v[82:85], v2 offset:6688
	ds_read_b128 v[158:161], v2 offset:64
	ds_read_b128 v[162:165], v2 offset:96
	ds_read_b128 v[86:89], v2 offset:6720
	ds_read_b128 v[90:93], v2 offset:6752
	ds_read_b128 v[194:197], v2 offset:128
	ds_read_b128 v[208:211], v2 offset:160
	ds_read_b128 v[94:97], v2 offset:6784
	ds_read_b128 v[166:169], v2 offset:6816
	v_xor_b32_e32 v16, 32, v242
	v_cmp_lt_i32_e32 vcc, v16, v17
	s_nop 1
	v_cndmask_b32_e32 v2, v242, v16, vcc
	v_lshlrev_b32_e32 v16, 2, v2
	v_add_u32_e32 v2, s26, v206
	s_waitcnt lgkmcnt(9)
	v_mfma_f32_32x32x16_bf16 v[66:81], v[12:15], v[134:137], v[50:65]
	s_waitcnt lgkmcnt(8)
	v_mfma_f32_32x32x16_bf16 v[66:81], v[82:85], v[138:141], v[66:81]
	s_waitcnt lgkmcnt(5)
	v_mfma_f32_32x32x16_bf16 v[66:81], v[86:89], v[142:145], v[66:81]
	s_waitcnt lgkmcnt(4)
	v_mfma_f32_32x32x16_bf16 v[66:81], v[90:93], v[146:149], v[66:81]
	s_waitcnt lgkmcnt(1)
	v_mfma_f32_32x32x16_bf16 v[66:81], v[94:97], v[150:153], v[66:81]
	s_waitcnt lgkmcnt(0)
	v_mfma_f32_32x32x16_bf16 v[66:81], v[166:169], v[154:157], v[66:81]
	v_mfma_f32_32x32x16_bf16 v[82:97], v[4:7], v[134:137], v[50:65]
	v_mfma_f32_32x32x16_bf16 v[82:97], v[8:11], v[138:141], v[82:97]
	ds_read_b64_tr_b16 v[174:175], v2 offset:13312
	ds_read_b64_tr_b16 v[176:177], v2 offset:13824
	ds_read_b64_tr_b16 v[170:171], v2 offset:14336
	ds_read_b64_tr_b16 v[172:173], v2 offset:14848
	ds_read_b64_tr_b16 v[166:167], v2 offset:15360
	ds_read_b64_tr_b16 v[168:169], v2 offset:15872
	ds_read_b64_tr_b16 v[8:9], v2 offset:16384
	ds_read_b64_tr_b16 v[10:11], v2 offset:16896
	v_mfma_f32_32x32x16_bf16 v[82:97], v[158:161], v[142:145], v[82:97]
	v_mfma_f32_32x32x16_bf16 v[82:97], v[162:165], v[146:149], v[82:97]
	ds_read_b64_tr_b16 v[162:163], v2 offset:17408
	ds_read_b64_tr_b16 v[164:165], v2 offset:17920
	ds_read_b64_tr_b16 v[158:159], v2 offset:18432
	ds_read_b64_tr_b16 v[160:161], v2 offset:18944
	ds_read_b64_tr_b16 v[12:13], v2 offset:19456
	ds_read_b64_tr_b16 v[14:15], v2 offset:19968
	ds_read_b64_tr_b16 v[4:5], v2 offset:20480
	ds_read_b64_tr_b16 v[6:7], v2 offset:20992
	v_mfma_f32_32x32x16_bf16 v[82:97], v[194:197], v[150:153], v[82:97]
	v_mfma_f32_32x32x16_bf16 v[82:97], v[208:211], v[154:157], v[82:97]
	s_nop 11
	v_max3_f32 v2, v82, v83, v84
	v_max3_f32 v194, v66, v67, v68
	v_max3_f32 v2, v2, v85, v86
	v_max3_f32 v194, v194, v69, v70
	v_max3_f32 v2, v2, v87, v88
	v_max3_f32 v194, v194, v71, v72
	v_max3_f32 v2, v2, v89, v90
	v_max3_f32 v194, v194, v73, v74
	v_max3_f32 v2, v2, v91, v92
	v_max3_f32 v194, v194, v75, v76
	v_max3_f32 v2, v2, v93, v94
	v_max3_f32 v194, v194, v77, v78
	v_max3_f32 v2, v2, v95, v96
	v_max3_f32 v194, v194, v79, v80
	v_max_f32_e32 v195, v97, v81
	v_max3_f32 v2, v2, v194, v195
	ds_bpermute_b32 v194, v16, v2
	s_cmp_lg_u32 s73, 0
	s_waitcnt lgkmcnt(0)
	v_max_f32_e32 v208, v2, v194
	s_cbranch_scc0 .Lmla_f_first
	v_cmp_lt_f32_e32 vcc, s81, v208
	s_cbranch_vccz .LBB0_726
	v_max_f32_e32 v2, v208, v208
	v_max_f32_e32 v2, 0, v2
	s_branch .Lmla_f_resc
.Lmla_f_first:
	v_mov_b32_e32 v2, v208
.Lmla_f_resc:
	v_exp_f32_e64 v52, -v2
	v_add_f32_e32 v193, v193, v2
	v_xor_b32_e32 v50, 0x80000000, v193
	v_pk_add_f32 v[82:83], v[82:83], v[2:3] op_sel_hi:[1,0] neg_lo:[0,1] neg_hi:[0,1]
	v_pk_add_f32 v[66:67], v[66:67], v[2:3] op_sel_hi:[1,0] neg_lo:[0,1] neg_hi:[0,1]
	v_pk_add_f32 v[84:85], v[84:85], v[2:3] op_sel_hi:[1,0] neg_lo:[0,1] neg_hi:[0,1]
	v_pk_add_f32 v[68:69], v[68:69], v[2:3] op_sel_hi:[1,0] neg_lo:[0,1] neg_hi:[0,1]
	v_pk_add_f32 v[86:87], v[86:87], v[2:3] op_sel_hi:[1,0] neg_lo:[0,1] neg_hi:[0,1]
	v_pk_add_f32 v[70:71], v[70:71], v[2:3] op_sel_hi:[1,0] neg_lo:[0,1] neg_hi:[0,1]
	v_pk_add_f32 v[88:89], v[88:89], v[2:3] op_sel_hi:[1,0] neg_lo:[0,1] neg_hi:[0,1]
	v_pk_add_f32 v[72:73], v[72:73], v[2:3] op_sel_hi:[1,0] neg_lo:[0,1] neg_hi:[0,1]
	v_pk_add_f32 v[90:91], v[90:91], v[2:3] op_sel_hi:[1,0] neg_lo:[0,1] neg_hi:[0,1]
	v_pk_add_f32 v[74:75], v[74:75], v[2:3] op_sel_hi:[1,0] neg_lo:[0,1] neg_hi:[0,1]
	v_pk_add_f32 v[92:93], v[92:93], v[2:3] op_sel_hi:[1,0] neg_lo:[0,1] neg_hi:[0,1]
	v_pk_add_f32 v[76:77], v[76:77], v[2:3] op_sel_hi:[1,0] neg_lo:[0,1] neg_hi:[0,1]
	v_pk_add_f32 v[94:95], v[94:95], v[2:3] op_sel_hi:[1,0] neg_lo:[0,1] neg_hi:[0,1]
	v_pk_add_f32 v[78:79], v[78:79], v[2:3] op_sel_hi:[1,0] neg_lo:[0,1] neg_hi:[0,1]
	v_pk_add_f32 v[96:97], v[96:97], v[2:3] op_sel_hi:[1,0] neg_lo:[0,1] neg_hi:[0,1]
	v_pk_add_f32 v[80:81], v[80:81], v[2:3] op_sel_hi:[1,0] neg_lo:[0,1] neg_hi:[0,1]
	v_pk_mul_f32 v[48:49], v[48:49], v[52:53] op_sel_hi:[1,0]
	v_pk_mul_f32 v[46:47], v[46:47], v[52:53] op_sel_hi:[1,0]
	v_pk_mul_f32 v[44:45], v[44:45], v[52:53] op_sel_hi:[1,0]
	v_pk_mul_f32 v[42:43], v[42:43], v[52:53] op_sel_hi:[1,0]
	v_pk_mul_f32 v[40:41], v[40:41], v[52:53] op_sel_hi:[1,0]
	v_pk_mul_f32 v[38:39], v[38:39], v[52:53] op_sel_hi:[1,0]
	v_pk_mul_f32 v[36:37], v[36:37], v[52:53] op_sel_hi:[1,0]
	v_pk_mul_f32 v[34:35], v[34:35], v[52:53] op_sel_hi:[1,0]
	v_pk_mul_f32 v[32:33], v[32:33], v[52:53] op_sel_hi:[1,0]
	v_pk_mul_f32 v[30:31], v[30:31], v[52:53] op_sel_hi:[1,0]
	v_pk_mul_f32 v[28:29], v[28:29], v[52:53] op_sel_hi:[1,0]
	v_pk_mul_f32 v[26:27], v[26:27], v[52:53] op_sel_hi:[1,0]
	v_pk_mul_f32 v[24:25], v[24:25], v[52:53] op_sel_hi:[1,0]
	v_pk_mul_f32 v[22:23], v[22:23], v[52:53] op_sel_hi:[1,0]
	v_pk_mul_f32 v[20:21], v[20:21], v[52:53] op_sel_hi:[1,0]
	v_pk_mul_f32 v[18:19], v[18:19], v[52:53] op_sel_hi:[1,0]
	v_mul_f32_e32 v191, v191, v52
	v_mov_b32_e32 v51, v50
	v_mov_b32_e32 v52, v50
	v_mov_b32_e32 v53, v50
	v_mov_b32_e32 v54, v50
	v_mov_b32_e32 v55, v50
	v_mov_b32_e32 v56, v50
	v_mov_b32_e32 v57, v50
	v_mov_b32_e32 v58, v50
	v_mov_b32_e32 v59, v50
	v_mov_b32_e32 v60, v50
	v_mov_b32_e32 v61, v50
	v_mov_b32_e32 v62, v50
	v_mov_b32_e32 v63, v50
	v_mov_b32_e32 v64, v50
	v_mov_b32_e32 v65, v50

.LBB0_730:
	s_andn2_b64 vcc, exec, s[10:11]
	s_cbranch_vccnz .LBB0_695
	s_branch .LBB0_739
.LBB0_732:
	s_cmp_eq_u32 s70, 1
	s_mov_b64 s[26:27], -1
	s_cbranch_scc0 .LBB0_734
	s_waitcnt vmcnt(7)
	v_bfe_u32 v4, v102, 16, 1
	v_add3_u32 v4, v102, v4, s86
	s_waitcnt vmcnt(6)
	v_bfe_u32 v5, v106, 16, 1
	v_lshrrev_b32_e32 v4, 16, v4
	v_add3_u32 v5, v106, v5, s86
	v_and_or_b32 v4, v5, s87, v4
	s_waitcnt vmcnt(5)
	v_bfe_u32 v5, v110, 16, 1
	v_add3_u32 v5, v110, v5, s86
	s_waitcnt vmcnt(4)
	v_bfe_u32 v6, v114, 16, 1
	v_lshrrev_b32_e32 v5, 16, v5
	v_add3_u32 v6, v114, v6, s86
	v_and_or_b32 v5, v6, s87, v5
	s_waitcnt vmcnt(3)
	v_bfe_u32 v6, v118, 16, 1
	v_add3_u32 v6, v118, v6, s86
	s_waitcnt vmcnt(2)
	v_bfe_u32 v7, v122, 16, 1
	v_lshrrev_b32_e32 v6, 16, v6
	v_add3_u32 v7, v122, v7, s86
	v_and_or_b32 v6, v7, s87, v6
	s_waitcnt vmcnt(1)
	v_bfe_u32 v7, v126, 16, 1
	v_add3_u32 v7, v126, v7, s86
	s_waitcnt vmcnt(0)
	v_bfe_u32 v8, v130, 16, 1
	v_lshrrev_b32_e32 v7, 16, v7
	v_add3_u32 v8, v130, v8, s86
	v_and_or_b32 v7, v8, s87, v7
	global_store_dwordx4 v[182:183], v[4:7], off
	v_bfe_u32 v8, v131, 16, 1
	v_add3_u32 v8, v131, v8, s86
	v_bfe_u32 v4, v103, 16, 1
	v_add3_u32 v4, v103, v4, s86
	v_bfe_u32 v5, v107, 16, 1
	v_lshrrev_b32_e32 v4, 16, v4
	v_add3_u32 v5, v107, v5, s86
	v_and_or_b32 v4, v5, s87, v4
	v_bfe_u32 v5, v111, 16, 1
	v_add3_u32 v5, v111, v5, s86
	v_bfe_u32 v6, v115, 16, 1
	v_lshrrev_b32_e32 v5, 16, v5
	v_add3_u32 v6, v115, v6, s86
	v_and_or_b32 v5, v6, s87, v5
	v_bfe_u32 v6, v119, 16, 1
	v_add3_u32 v6, v119, v6, s86
	v_bfe_u32 v7, v123, 16, 1
	v_lshrrev_b32_e32 v6, 16, v6
	v_add3_u32 v7, v123, v7, s86
	v_and_or_b32 v6, v7, s87, v6
	v_bfe_u32 v7, v127, 16, 1
	v_add3_u32 v7, v127, v7, s86
	v_lshrrev_b32_e32 v7, 16, v7
	v_and_or_b32 v7, v8, s87, v7
	global_store_dwordx4 v[182:183], v[4:7], off offset:1024
	v_bfe_u32 v8, v132, 16, 1
	v_add3_u32 v8, v132, v8, s86
	v_bfe_u32 v4, v104, 16, 1
	v_add3_u32 v4, v104, v4, s86
	v_bfe_u32 v5, v108, 16, 1
	v_lshrrev_b32_e32 v4, 16, v4
	v_add3_u32 v5, v108, v5, s86
	v_and_or_b32 v4, v5, s87, v4
	v_bfe_u32 v5, v112, 16, 1
	v_add3_u32 v5, v112, v5, s86
	v_bfe_u32 v6, v116, 16, 1
	v_lshrrev_b32_e32 v5, 16, v5
	v_add3_u32 v6, v116, v6, s86
	v_and_or_b32 v5, v6, s87, v5
	v_bfe_u32 v6, v120, 16, 1
	v_add3_u32 v6, v120, v6, s86
	v_bfe_u32 v7, v124, 16, 1
	v_lshrrev_b32_e32 v6, 16, v6
	v_add3_u32 v7, v124, v7, s86
	v_and_or_b32 v6, v7, s87, v6
	v_bfe_u32 v7, v128, 16, 1
	v_add3_u32 v7, v128, v7, s86
	v_lshrrev_b32_e32 v7, 16, v7
	v_and_or_b32 v7, v8, s87, v7
	global_store_dwordx4 v[182:183], v[4:7], off offset:2048
	v_bfe_u32 v8, v133, 16, 1
	v_add3_u32 v8, v133, v8, s86
	v_bfe_u32 v4, v105, 16, 1
	v_add3_u32 v4, v105, v4, s86
	v_bfe_u32 v5, v109, 16, 1
	v_lshrrev_b32_e32 v4, 16, v4
	v_add3_u32 v5, v109, v5, s86
	v_and_or_b32 v4, v5, s87, v4
	v_bfe_u32 v5, v113, 16, 1
	v_add3_u32 v5, v113, v5, s86
	v_bfe_u32 v6, v117, 16, 1
	v_lshrrev_b32_e32 v5, 16, v5
	v_add3_u32 v6, v117, v6, s86
	v_and_or_b32 v5, v6, s87, v5
	v_bfe_u32 v6, v121, 16, 1
	v_add3_u32 v6, v121, v6, s86
	v_bfe_u32 v7, v125, 16, 1
	v_lshrrev_b32_e32 v6, 16, v6
	v_add3_u32 v7, v125, v7, s86
	v_and_or_b32 v6, v7, s87, v6
	v_bfe_u32 v7, v129, 16, 1
	v_add3_u32 v7, v129, v7, s86
	v_lshrrev_b32_e32 v7, 16, v7
	v_and_or_b32 v7, v8, s87, v7
	global_store_dwordx4 v[182:183], v[4:7], off offset:3072
	s_mov_b64 s[26:27], 0

.LBB0_839:
	v_exp_f32_e32 v194, v162
	v_exp_f32_e32 v195, v146
	v_exp_f32_e32 v2, v163
	v_exp_f32_e32 v12, v147
	v_exp_f32_e32 v196, v148
	v_add_f32_e32 v13, v195, v194
	v_exp_f32_e32 v14, v149
	v_pk_add_f32 v[4:5], v[12:13], v[2:3]
	v_exp_f32_e32 v13, v164
	v_pk_add_f32 v[10:11], v[4:5], v[4:5] op_sel_hi:[0,1]
	v_exp_f32_e32 v10, v165
	v_exp_f32_e32 v227, v116
	v_add_f32_e32 v15, v196, v13
	v_exp_f32_e32 v229, v117
	v_pk_add_f32 v[4:5], v[14:15], v[10:11]
	v_exp_f32_e32 v11, v166
	v_pk_add_f32 v[116:117], v[4:5], v[4:5] op_sel_hi:[0,1]
	v_exp_f32_e32 v15, v150
	v_exp_f32_e32 v217, v118
	v_exp_f32_e32 v116, v167
	v_exp_f32_e32 v118, v151
	v_exp_f32_e32 v221, v119
	v_add_f32_e32 v119, v15, v11
	v_exp_f32_e32 v224, v136
	v_pk_add_f32 v[4:5], v[118:119], v[116:117]
	v_exp_f32_e32 v225, v120
	v_exp_f32_e32 v136, v121
	v_pk_add_f32 v[120:121], v[4:5], v[4:5] op_sel_hi:[0,1]
	v_exp_f32_e32 v117, v168
	v_exp_f32_e32 v119, v152
	v_exp_f32_e32 v218, v130
	v_exp_f32_e32 v120, v169
	v_exp_f32_e32 v130, v153
	v_exp_f32_e32 v222, v131
	v_add_f32_e32 v131, v119, v117
	v_exp_f32_e32 v219, v114
	v_pk_add_f32 v[6:7], v[130:131], v[120:121]
	v_exp_f32_e32 v223, v115
	v_exp_f32_e32 v220, v135
	v_exp_f32_e32 v135, v137
	v_exp_f32_e32 v137, v138
	v_exp_f32_e32 v138, v122
	v_exp_f32_e32 v122, v139
	v_exp_f32_e32 v139, v141
	v_exp_f32_e32 v141, v143
	v_exp_f32_e32 v143, v145
	v_pk_add_f32 v[114:115], v[6:7], v[6:7] op_sel_hi:[0,1]
	v_exp_f32_e32 v131, v170
	v_exp_f32_e32 v145, v154
	v_exp_f32_e32 v114, v171
	v_exp_f32_e32 v16, v155
	v_exp_f32_e32 v226, v132
	v_add_f32_e32 v17, v145, v131
	v_exp_f32_e32 v228, v133
	v_pk_add_f32 v[8:9], v[16:17], v[114:115]
	v_exp_f32_e32 v17, v172
	v_pk_add_f32 v[132:133], v[8:9], v[8:9] op_sel_hi:[0,1]
	v_exp_f32_e32 v172, v156
	v_exp_f32_e32 v132, v173
	v_exp_f32_e32 v170, v157
	v_add_u32_e32 v173, s6, v201
	v_add_f32_e32 v171, v172, v17
	v_exp_f32_e32 v134, v134
	ds_read_b64_tr_b16 v[146:147], v173 offset:9216
	ds_read_b64_tr_b16 v[148:149], v173 offset:9728
	v_pk_add_f32 v[150:151], v[170:171], v[132:133]
	v_exp_f32_e32 v115, v174
	v_pk_add_f32 v[162:163], v[150:151], v[150:151] op_sel_hi:[0,1]
	v_exp_f32_e32 v133, v158
	v_exp_f32_e32 v162, v175
	v_exp_f32_e32 v158, v159
	v_cvt_pk_bf16_f32 v4, v218, v222
	v_cvt_pk_bf16_f32 v5, v226, v228
	v_cvt_pk_bf16_f32 v6, v134, v220
	v_cvt_pk_bf16_f32 v7, v224, v135
	v_cvt_pk_bf16_f32 v154, v194, v2
	v_cvt_pk_bf16_f32 v155, v13, v10
	v_cvt_pk_bf16_f32 v156, v11, v116
	v_cvt_pk_bf16_f32 v157, v117, v120
	s_waitcnt lgkmcnt(0)
	v_mfma_f32_32x32x16_bf16 v[18:33], v[146:149], v[4:7], v[18:33]
	v_add_f32_e32 v159, v133, v115
	v_add_f32_e64 v116, v158, v162
	v_add_f32_e64 v117, v159, v163
	v_exp_f32_e32 v140, v140
	v_pk_add_f32 v[120:121], v[116:117], v[116:117] op_sel_hi:[0,1]
	v_exp_f32_e32 v142, v142
	v_exp_f32_e32 v144, v144
	ds_read_b64_tr_b16 v[150:151], v173 offset:10240
	ds_read_b64_tr_b16 v[152:153], v173 offset:10752
	v_mfma_f32_32x32x16_bf16 v[34:49], v[146:149], v[154:157], v[34:49]
	v_exp_f32_e32 v2, v176
	v_exp_f32_e32 v120, v177
	v_cvt_pk_bf16_f32 v8, v137, v122
	v_cvt_pk_bf16_f32 v9, v140, v139
	v_cvt_pk_bf16_f32 v10, v142, v141
	v_cvt_pk_bf16_f32 v11, v144, v143
	v_cvt_pk_bf16_f32 v146, v131, v114
	v_cvt_pk_bf16_f32 v147, v17, v132
	v_cvt_pk_bf16_f32 v148, v115, v162
	v_cvt_pk_bf16_f32 v149, v2, v120
	s_waitcnt lgkmcnt(0)
	v_mfma_f32_32x32x16_bf16 v[18:33], v[150:153], v[8:11], v[18:33]
	ds_read_b64_tr_b16 v[162:163], v173 offset:11264
	ds_read_b64_tr_b16 v[164:165], v173 offset:11776
	v_cvt_pk_bf16_f32 v114, v219, v223
	v_cvt_pk_bf16_f32 v115, v227, v229
	v_cvt_pk_bf16_f32 v116, v217, v221
	v_cvt_pk_bf16_f32 v117, v225, v136
	v_cvt_pk_bf16_f32 v166, v195, v12
	v_cvt_pk_bf16_f32 v167, v196, v14
	v_mfma_f32_32x32x16_bf16 v[34:49], v[150:153], v[146:149], v[34:49]
	v_cvt_pk_bf16_f32 v168, v15, v118
	v_cvt_pk_bf16_f32 v169, v119, v130
	v_exp_f32_e32 v17, v123
	ds_read_b64_tr_b16 v[150:151], v173 offset:12288
	ds_read_b64_tr_b16 v[152:153], v173 offset:12800
	v_exp_f32_e32 v123, v124
	v_exp_f32_e32 v132, v125
	v_exp_f32_e32 v159, v126
	s_waitcnt lgkmcnt(2)
	v_mfma_f32_32x32x16_bf16 v[18:33], v[162:165], v[114:117], v[18:33]
	v_exp_f32_e32 v119, v127
	v_exp_f32_e32 v160, v160
	v_exp_f32_e32 v118, v161
	v_cvt_pk_bf16_f32 v12, v138, v17
	v_cvt_pk_bf16_f32 v13, v123, v132
	v_cvt_pk_bf16_f32 v14, v159, v119
	v_cvt_pk_bf16_f32 v124, v145, v16
	v_mfma_f32_32x32x16_bf16 v[34:49], v[162:165], v[166:169], v[34:49]
	v_exp_f32_e32 v162, v128
	v_exp_f32_e32 v163, v129
	v_cvt_pk_bf16_f32 v125, v172, v170
	v_cvt_pk_bf16_f32 v126, v133, v158
	v_cvt_pk_bf16_f32 v127, v160, v118
	v_cvt_pk_bf16_f32 v15, v162, v163
	v_add_f32_e32 v17, v17, v122
	s_waitcnt lgkmcnt(0)
	v_mfma_f32_32x32x16_bf16 v[34:49], v[150:153], v[124:127], v[34:49]
	s_add_i32 s0, s91, 1
	s_and_b32 s91, s0, 3
	s_add_i32 s0, s74, 1
	s_and_b32 s74, s0, 3
	s_add_i32 s10, s10, 1
	s_cmp_eq_u32 s8, s10
	v_mfma_f32_32x32x16_bf16 v[18:33], v[150:153], v[12:15], v[18:33]
	ds_read_b64_tr_b16 v[128:129], v173 offset:13312
	ds_read_b64_tr_b16 v[130:131], v173 offset:13824
	ds_read_b64_tr_b16 v[150:151], v173 offset:14336
	ds_read_b64_tr_b16 v[152:153], v173 offset:14848
	s_waitcnt lgkmcnt(2)
	v_mfma_f32_32x32x16_bf16 v[50:65], v[128:131], v[4:7], v[50:65]
	v_add_f32_e32 v4, v219, v218
	v_add_f32_e32 v5, v223, v222
	v_add_f32_e32 v4, v5, v4
	v_add_f32_e32 v5, v227, v226
	v_add_f32_e32 v4, v5, v4
	v_add_f32_e32 v5, v229, v228
	v_mfma_f32_32x32x16_bf16 v[66:81], v[128:131], v[154:157], v[66:81]
	v_add_f32_e32 v4, v5, v4
	v_add_f32_e32 v5, v217, v134
	v_add_f32_e32 v4, v5, v4
	v_add_f32_e32 v5, v221, v220
	s_waitcnt lgkmcnt(0)
	v_mfma_f32_32x32x16_bf16 v[50:65], v[150:153], v[8:11], v[50:65]
	v_add_f32_e32 v8, v5, v4
	ds_read_b64_tr_b16 v[4:5], v173 offset:15360
	ds_read_b64_tr_b16 v[6:7], v173 offset:15872
	v_add_f32_e32 v9, v225, v224
	v_add_f32_e32 v8, v9, v8
	v_add_f32_e32 v9, v136, v135
	v_add_f32_e32 v8, v9, v8
	v_add_f32_e32 v9, v138, v137
	v_mfma_f32_32x32x16_bf16 v[66:81], v[150:153], v[146:149], v[66:81]
	v_add_f32_e32 v16, v9, v8
	ds_read_b64_tr_b16 v[8:9], v173 offset:16384
	ds_read_b64_tr_b16 v[10:11], v173 offset:16896
	v_add_f32_e32 v16, v17, v16
	v_add_f32_e32 v17, v123, v140
	v_add_f32_e32 v16, v17, v16
	v_add_f32_e32 v17, v132, v139
	v_add_f32_e32 v16, v17, v16
	s_waitcnt lgkmcnt(2)
	v_mfma_f32_32x32x16_bf16 v[50:65], v[4:7], v[114:117], v[50:65]
	v_add_f32_e32 v17, v159, v142
	s_waitcnt vmcnt(6) lgkmcnt(0)
	s_barrier
	v_mfma_f32_32x32x16_bf16 v[66:81], v[4:7], v[166:169], v[66:81]
	v_add_f32_e32 v4, v17, v16
	v_add_f32_e32 v5, v119, v141
	v_add_f32_e32 v4, v5, v4
	v_add_f32_e32 v5, v162, v144
	v_add_f32_e32 v4, v5, v4
	v_add_f32_e32 v5, v163, v143
	v_add_f32_e32 v4, v5, v4
	s_waitcnt lgkmcnt(0)
	v_mfma_f32_32x32x16_bf16 v[50:65], v[8:11], v[12:15], v[50:65]
	v_add_f32_e32 v119, v160, v2
	v_add_f32_e32 v214, v214, v4
	v_add_f32_e64 v4, v118, v120
	v_add_f32_e64 v5, v119, v121
	v_add_f32_e32 v2, v4, v5
	v_add_f32_e32 v209, v209, v2
	v_mfma_f32_32x32x16_bf16 v[66:81], v[8:11], v[124:127], v[66:81]
	s_cbranch_scc1 .LBB0_868

.LBB0_851:
	s_mul_i32 s2, s74, 0x4400
	s_add_i32 s6, s2, 0
	v_add_u32_e32 v5, s6, v207
	ds_read_b128 v[6:9], v5 offset:4608
	ds_read_b128 v[10:13], v5
	ds_read_b128 v[14:17], v5 offset:32
	ds_read_b128 v[146:149], v5 offset:4640
	v_and_b32_e32 v4, 64, v242
	v_xor_b32_e32 v2, 32, v242
	v_add_u32_e32 v4, 64, v4
	v_cmp_lt_i32_e32 vcc, v2, v4
	s_cmp_lg_u32 s10, 0
	s_cselect_b64 s[2:3], -1, 0
	v_cndmask_b32_e32 v2, v242, v2, vcc
	v_lshlrev_b32_e32 v4, 2, v2
	s_waitcnt lgkmcnt(2)
	v_mfma_f32_32x32x16_bf16 v[130:145], v[10:13], v[178:181], v[98:113]
	s_and_b64 vcc, exec, s[2:3]
	v_mfma_f32_32x32x16_bf16 v[114:129], v[6:9], v[178:181], v[98:113]
	s_waitcnt lgkmcnt(1)
	v_mfma_f32_32x32x16_bf16 v[130:145], v[14:17], v[182:185], v[130:145]
	s_waitcnt lgkmcnt(0)
	v_mfma_f32_32x32x16_bf16 v[114:129], v[146:149], v[182:185], v[114:129]
	s_nop 9
	v_max3_f32 v2, v130, v131, v132
	v_max3_f32 v2, v2, v133, v134
	v_max3_f32 v2, v2, v135, v136
	v_max3_f32 v2, v2, v137, v138
	v_max3_f32 v2, v2, v139, v140
	v_max3_f32 v2, v2, v141, v142
	v_max3_f32 v6, v114, v115, v116
	v_max3_f32 v6, v6, v117, v118
	v_max3_f32 v6, v6, v119, v120
	v_max3_f32 v6, v6, v121, v122
	v_max3_f32 v6, v6, v123, v124
	v_max3_f32 v6, v6, v125, v126
	v_max3_f32 v2, v2, v143, v144
	v_max3_f32 v6, v6, v127, v128
	v_max_f32_e32 v7, v145, v129
	v_max3_f32 v2, v2, v6, v7
	ds_bpermute_b32 v6, v4, v2
	s_waitcnt lgkmcnt(0)
	v_max_f32_e32 v6, v2, v6
	s_cbranch_vccz .Ldf0_first
	v_cmp_lt_f32_e32 vcc, s11, v6
	s_cbranch_vccz .LBB0_858
	v_max_f32_e32 v2, v6, v6
	v_max_f32_e32 v2, 0, v2
	s_branch .Ldf0_resc
.Ldf0_first:
	v_mov_b32_e32 v2, v6
.Ldf0_resc:
	v_exp_f32_e64 v6, -v2
	v_add_f32_e32 v216, v216, v2
	v_xor_b32_e32 v98, 0x80000000, v216
	v_pk_add_f32 v[130:131], v[130:131], v[2:3] op_sel_hi:[1,0] neg_lo:[0,1] neg_hi:[0,1]
	v_mul_f32_e32 v214, v214, v6
	v_pk_add_f32 v[114:115], v[114:115], v[2:3] op_sel_hi:[1,0] neg_lo:[0,1] neg_hi:[0,1]
	v_pk_add_f32 v[132:133], v[132:133], v[2:3] op_sel_hi:[1,0] neg_lo:[0,1] neg_hi:[0,1]
	v_pk_add_f32 v[116:117], v[116:117], v[2:3] op_sel_hi:[1,0] neg_lo:[0,1] neg_hi:[0,1]
	v_pk_add_f32 v[134:135], v[134:135], v[2:3] op_sel_hi:[1,0] neg_lo:[0,1] neg_hi:[0,1]
	v_pk_add_f32 v[118:119], v[118:119], v[2:3] op_sel_hi:[1,0] neg_lo:[0,1] neg_hi:[0,1]
	v_pk_add_f32 v[136:137], v[136:137], v[2:3] op_sel_hi:[1,0] neg_lo:[0,1] neg_hi:[0,1]
	v_pk_add_f32 v[120:121], v[120:121], v[2:3] op_sel_hi:[1,0] neg_lo:[0,1] neg_hi:[0,1]
	v_pk_add_f32 v[138:139], v[138:139], v[2:3] op_sel_hi:[1,0] neg_lo:[0,1] neg_hi:[0,1]
	v_pk_add_f32 v[122:123], v[122:123], v[2:3] op_sel_hi:[1,0] neg_lo:[0,1] neg_hi:[0,1]
	v_pk_add_f32 v[140:141], v[140:141], v[2:3] op_sel_hi:[1,0] neg_lo:[0,1] neg_hi:[0,1]
	v_pk_add_f32 v[124:125], v[124:125], v[2:3] op_sel_hi:[1,0] neg_lo:[0,1] neg_hi:[0,1]
	v_pk_add_f32 v[142:143], v[142:143], v[2:3] op_sel_hi:[1,0] neg_lo:[0,1] neg_hi:[0,1]
	v_pk_add_f32 v[126:127], v[126:127], v[2:3] op_sel_hi:[1,0] neg_lo:[0,1] neg_hi:[0,1]
	v_pk_add_f32 v[144:145], v[144:145], v[2:3] op_sel_hi:[1,0] neg_lo:[0,1] neg_hi:[0,1]
	v_pk_add_f32 v[128:129], v[128:129], v[2:3] op_sel_hi:[1,0] neg_lo:[0,1] neg_hi:[0,1]
	v_pk_mul_f32 v[32:33], v[32:33], v[6:7] op_sel_hi:[1,0]
	v_pk_mul_f32 v[30:31], v[30:31], v[6:7] op_sel_hi:[1,0]
	v_pk_mul_f32 v[28:29], v[28:29], v[6:7] op_sel_hi:[1,0]
	v_pk_mul_f32 v[26:27], v[26:27], v[6:7] op_sel_hi:[1,0]
	v_pk_mul_f32 v[24:25], v[24:25], v[6:7] op_sel_hi:[1,0]
	v_pk_mul_f32 v[22:23], v[22:23], v[6:7] op_sel_hi:[1,0]
	v_pk_mul_f32 v[20:21], v[20:21], v[6:7] op_sel_hi:[1,0]
	v_pk_mul_f32 v[18:19], v[18:19], v[6:7] op_sel_hi:[1,0]
	v_pk_mul_f32 v[64:65], v[64:65], v[6:7] op_sel_hi:[1,0]
	v_pk_mul_f32 v[62:63], v[62:63], v[6:7] op_sel_hi:[1,0]
	v_pk_mul_f32 v[60:61], v[60:61], v[6:7] op_sel_hi:[1,0]
	v_pk_mul_f32 v[58:59], v[58:59], v[6:7] op_sel_hi:[1,0]
	v_pk_mul_f32 v[56:57], v[56:57], v[6:7] op_sel_hi:[1,0]
	v_pk_mul_f32 v[54:55], v[54:55], v[6:7] op_sel_hi:[1,0]
	v_pk_mul_f32 v[52:53], v[52:53], v[6:7] op_sel_hi:[1,0]
	v_pk_mul_f32 v[50:51], v[50:51], v[6:7] op_sel_hi:[1,0]
	v_mov_b32_e32 v99, v98
	v_mov_b32_e32 v100, v98
	v_mov_b32_e32 v101, v98
	v_mov_b32_e32 v102, v98
	v_mov_b32_e32 v103, v98
	v_mov_b32_e32 v104, v98
	v_mov_b32_e32 v105, v98
	v_mov_b32_e32 v106, v98
	v_mov_b32_e32 v107, v98
	v_mov_b32_e32 v108, v98
	v_mov_b32_e32 v109, v98
	v_mov_b32_e32 v110, v98
	v_mov_b32_e32 v111, v98
	v_mov_b32_e32 v112, v98
	v_mov_b32_e32 v113, v98
.LBB0_858:
	ds_read_b128 v[6:9], v5 offset:64
	ds_read_b128 v[10:13], v5 offset:96
	ds_read_b128 v[14:17], v5 offset:4672
	ds_read_b128 v[194:197], v5 offset:4704
	s_waitcnt lgkmcnt(3)
	v_mfma_f32_32x32x16_bf16 v[162:177], v[6:9], v[186:189], v[82:97]
	s_and_b64 vcc, exec, s[2:3]
	s_waitcnt lgkmcnt(1)
	v_mfma_f32_32x32x16_bf16 v[146:161], v[14:17], v[186:189], v[82:97]
	v_mfma_f32_32x32x16_bf16 v[162:177], v[10:13], v[190:193], v[162:177]
	s_waitcnt lgkmcnt(0)
	v_mfma_f32_32x32x16_bf16 v[146:161], v[194:197], v[190:193], v[146:161]
	s_nop 9
	v_max3_f32 v2, v162, v163, v164
	v_max3_f32 v2, v2, v165, v166
	v_max3_f32 v2, v2, v167, v168
	v_max3_f32 v2, v2, v169, v170
	v_max3_f32 v2, v2, v171, v172
	v_max3_f32 v2, v2, v173, v174
	v_max3_f32 v5, v146, v147, v148
	v_max3_f32 v5, v5, v149, v150
	v_max3_f32 v5, v5, v151, v152
	v_max3_f32 v5, v5, v153, v154
	v_max3_f32 v5, v5, v155, v156
	v_max3_f32 v5, v5, v157, v158
	v_max3_f32 v2, v2, v175, v176
	v_max3_f32 v5, v5, v159, v160
	v_max_f32_e32 v6, v177, v161
	v_max3_f32 v2, v2, v5, v6
	ds_bpermute_b32 v4, v4, v2
	s_waitcnt lgkmcnt(0)
	v_max_f32_e32 v4, v2, v4
	s_cbranch_vccz .Ldf1_first
	v_cmp_lt_f32_e32 vcc, s11, v4
	s_cbranch_vccz .LBB0_839
	v_max_f32_e32 v2, v4, v4
	v_max_f32_e32 v2, 0, v2
	s_branch .Ldf1_resc
.Ldf1_first:
	v_mov_b32_e32 v2, v4
.Ldf1_resc:
	v_exp_f32_e64 v4, -v2
	v_add_f32_e32 v215, v215, v2
	v_xor_b32_e32 v82, 0x80000000, v215
	v_pk_add_f32 v[162:163], v[162:163], v[2:3] op_sel_hi:[1,0] neg_lo:[0,1] neg_hi:[0,1]
	v_mul_f32_e32 v209, v209, v4
	v_pk_add_f32 v[146:147], v[146:147], v[2:3] op_sel_hi:[1,0] neg_lo:[0,1] neg_hi:[0,1]
	v_pk_add_f32 v[164:165], v[164:165], v[2:3] op_sel_hi:[1,0] neg_lo:[0,1] neg_hi:[0,1]
	v_pk_add_f32 v[148:149], v[148:149], v[2:3] op_sel_hi:[1,0] neg_lo:[0,1] neg_hi:[0,1]
	v_pk_add_f32 v[166:167], v[166:167], v[2:3] op_sel_hi:[1,0] neg_lo:[0,1] neg_hi:[0,1]
	v_pk_add_f32 v[150:151], v[150:151], v[2:3] op_sel_hi:[1,0] neg_lo:[0,1] neg_hi:[0,1]
	v_pk_add_f32 v[168:169], v[168:169], v[2:3] op_sel_hi:[1,0] neg_lo:[0,1] neg_hi:[0,1]
	v_pk_add_f32 v[152:153], v[152:153], v[2:3] op_sel_hi:[1,0] neg_lo:[0,1] neg_hi:[0,1]
	v_pk_add_f32 v[170:171], v[170:171], v[2:3] op_sel_hi:[1,0] neg_lo:[0,1] neg_hi:[0,1]
	v_pk_add_f32 v[154:155], v[154:155], v[2:3] op_sel_hi:[1,0] neg_lo:[0,1] neg_hi:[0,1]
	v_pk_add_f32 v[172:173], v[172:173], v[2:3] op_sel_hi:[1,0] neg_lo:[0,1] neg_hi:[0,1]
	v_pk_add_f32 v[156:157], v[156:157], v[2:3] op_sel_hi:[1,0] neg_lo:[0,1] neg_hi:[0,1]
	v_pk_add_f32 v[174:175], v[174:175], v[2:3] op_sel_hi:[1,0] neg_lo:[0,1] neg_hi:[0,1]
	v_pk_add_f32 v[158:159], v[158:159], v[2:3] op_sel_hi:[1,0] neg_lo:[0,1] neg_hi:[0,1]
	v_pk_add_f32 v[176:177], v[176:177], v[2:3] op_sel_hi:[1,0] neg_lo:[0,1] neg_hi:[0,1]
	v_pk_add_f32 v[160:161], v[160:161], v[2:3] op_sel_hi:[1,0] neg_lo:[0,1] neg_hi:[0,1]
	v_pk_mul_f32 v[48:49], v[48:49], v[4:5] op_sel_hi:[1,0]
	v_pk_mul_f32 v[46:47], v[46:47], v[4:5] op_sel_hi:[1,0]
	v_pk_mul_f32 v[44:45], v[44:45], v[4:5] op_sel_hi:[1,0]
	v_pk_mul_f32 v[42:43], v[42:43], v[4:5] op_sel_hi:[1,0]
	v_pk_mul_f32 v[40:41], v[40:41], v[4:5] op_sel_hi:[1,0]
	v_pk_mul_f32 v[38:39], v[38:39], v[4:5] op_sel_hi:[1,0]
	v_pk_mul_f32 v[36:37], v[36:37], v[4:5] op_sel_hi:[1,0]
	v_pk_mul_f32 v[34:35], v[34:35], v[4:5] op_sel_hi:[1,0]
	v_pk_mul_f32 v[80:81], v[80:81], v[4:5] op_sel_hi:[1,0]
	v_pk_mul_f32 v[78:79], v[78:79], v[4:5] op_sel_hi:[1,0]
	v_pk_mul_f32 v[76:77], v[76:77], v[4:5] op_sel_hi:[1,0]
	v_pk_mul_f32 v[74:75], v[74:75], v[4:5] op_sel_hi:[1,0]
	v_pk_mul_f32 v[72:73], v[72:73], v[4:5] op_sel_hi:[1,0]
	v_pk_mul_f32 v[70:71], v[70:71], v[4:5] op_sel_hi:[1,0]
	v_pk_mul_f32 v[68:69], v[68:69], v[4:5] op_sel_hi:[1,0]
	v_pk_mul_f32 v[66:67], v[66:67], v[4:5] op_sel_hi:[1,0]
	v_mov_b32_e32 v83, v82
	v_mov_b32_e32 v84, v82
	v_mov_b32_e32 v85, v82
	v_mov_b32_e32 v86, v82
	v_mov_b32_e32 v87, v82
	v_mov_b32_e32 v88, v82
	v_mov_b32_e32 v89, v82
	v_mov_b32_e32 v90, v82
	v_mov_b32_e32 v91, v82
	v_mov_b32_e32 v92, v82
	v_mov_b32_e32 v93, v82
	v_mov_b32_e32 v94, v82
	v_mov_b32_e32 v95, v82
	v_mov_b32_e32 v96, v82
	v_mov_b32_e32 v97, v82
	s_branch .LBB0_839
